# opt8 + first-round stagger of odd TG slot in conv1 and of waves 4-7 in VQ phase
# speedup vs baseline: 1.0112x; 1.0112x over previous
_Z11k_conv1_t14I3GeoILi64ELi16ELi3ELi2EEEvPKfPKDv8_DF16_S3_Pfiiii:
	s_getreg_b32 s60, hwreg(HW_REG_HW_ID, 16, 4)
	s_and_b32 s60, s60, 1
	s_cmp_eq_u32 s60, 0
	s_cbranch_scc1 .Lc1_nosleep
	s_cmp_lt_u32 s4, 4
	s_cbranch_scc0 .Lc1_nosleep
	s_sleep 54
.Lc1_nosleep:
	s_load_dwordx2 s[34:35], s[0:1], 0x0
	s_load_dwordx4 s[16:19], s[0:1], 0x20
	s_lshl_b32 s5, s3, 3
	v_readfirstlane_b32 s12, v0
	s_lshl_b32 s57, s2, 6
	s_add_i32 s54, s5, -1
	s_lshr_b32 s20, s12, 6
	s_waitcnt lgkmcnt(0)
	s_mul_i32 s28, s17, s16
	s_add_i32 s24, s57, -1
	s_add_i32 s56, s16, -1
	s_lshl_b32 s55, s4, 6
	s_ashr_i32 s29, s28, 31
	s_add_i32 s10, s20, s54
	s_cmpk_gt_u32 s12, 0x23f
	s_cselect_b64 s[6:7], -1, 0
	s_and_b64 s[8:9], s[6:7], exec
	s_cselect_b32 s23, -9, 0
	s_cselect_b32 s8, 8, 0
	s_add_i32 s10, s10, s23
	s_max_i32 s9, s10, 0
	s_or_b32 s8, s8, s55
	s_min_i32 s9, s9, s56
	s_mul_i32 s8, s8, s16
	s_add_i32 s8, s9, s8
	s_mul_i32 s36, s8, s17
	s_ashr_i32 s37, s36, 31
	s_lshl_b64 s[30:31], s[28:29], 2
	s_cmpk_gt_u32 s12, 0x13f
	s_cselect_b64 s[8:9], -1, 0
	s_and_b64 s[10:11], s[8:9], exec
	s_cselect_b32 s10, -9, 0
	v_mov_b32_e32 v1, v0
	s_cselect_b32 s11, 8, 0
	s_add_i32 s22, s20, s10
	s_add_i32 s22, s22, 4
	v_and_b32_e32 v1, 63, v1
	s_add_i32 s10, s22, s54
	v_or_b32_e32 v2, s57, v1
	s_max_i32 s10, s10, 0
	s_or_b32 s11, s11, s55
	v_ashrrev_i32_e32 v3, 31, v2
	s_min_i32 s10, s10, s56
	s_mul_i32 s11, s11, s16
	v_lshl_add_u64 v[4:5], v[2:3], 2, s[34:35]
	s_add_i32 s10, s10, s11
	v_lshl_add_u64 v[6:7], s[36:37], 2, v[4:5]
	s_mul_i32 s38, s10, s17
	v_lshl_add_u64 v[8:9], v[6:7], 0, s[30:31]
	s_ashr_i32 s39, s38, 31
	v_lshl_add_u64 v[10:11], v[8:9], 0, s[30:31]
	s_cmp_lt_u32 s12, 64
	v_lshl_add_u64 v[12:13], v[10:11], 0, s[30:31]
	s_cselect_b64 s[10:11], -1, 0
	v_lshl_add_u64 v[14:15], v[12:13], 0, s[30:31]
	s_and_b64 s[14:15], s[10:11], exec
	v_lshl_add_u64 v[16:17], v[14:15], 0, s[30:31]
	s_cselect_b32 s13, 0, -9
	v_lshl_add_u64 v[18:19], v[16:17], 0, s[30:31]
	s_cselect_b32 s14, 0, 8
	s_add_i32 s21, s20, s13
	v_lshl_add_u64 v[20:21], v[18:19], 0, s[30:31]
	global_load_dword v44, v[6:7], off
	global_load_dword v43, v[8:9], off
	global_load_dword v34, v[10:11], off
	global_load_dword v35, v[12:13], off
	global_load_dword v30, v[14:15], off
	global_load_dword v31, v[16:17], off
	global_load_dword v32, v[18:19], off
	global_load_dword v33, v[20:21], off
	v_lshl_add_u64 v[6:7], s[38:39], 2, v[4:5]
	s_add_i32 s21, s21, 8
	v_lshl_add_u64 v[8:9], v[6:7], 0, s[30:31]
	s_add_i32 s13, s21, s54
	v_lshl_add_u64 v[10:11], v[8:9], 0, s[30:31]
	s_max_i32 s13, s13, 0
	s_or_b32 s14, s14, s55
	v_lshl_add_u64 v[12:13], v[10:11], 0, s[30:31]
	s_min_i32 s13, s13, s56
	s_mul_i32 s14, s14, s16
	v_lshl_add_u64 v[14:15], v[12:13], 0, s[30:31]
	s_add_i32 s13, s13, s14
	v_lshl_add_u64 v[16:17], v[14:15], 0, s[30:31]
	s_mul_i32 s40, s13, s17
	v_lshl_add_u64 v[18:19], v[16:17], 0, s[30:31]
	s_ashr_i32 s41, s40, 31
	s_add_i32 s58, s20, s5
	v_lshl_add_u64 v[20:21], v[18:19], 0, s[30:31]
	global_load_dword v42, v[6:7], off
	global_load_dword v41, v[8:9], off
	global_load_dword v28, v[10:11], off
	global_load_dword v29, v[12:13], off
	global_load_dword v24, v[14:15], off
	global_load_dword v25, v[16:17], off
	global_load_dword v26, v[18:19], off
	global_load_dword v27, v[20:21], off
	v_lshl_add_u64 v[6:7], s[40:41], 2, v[4:5]
	s_add_i32 s13, s58, 2
	v_lshl_add_u64 v[8:9], v[6:7], 0, s[30:31]
	s_max_i32 s13, s13, 0
	s_or_b32 s14, s55, 8
	v_lshl_add_u64 v[10:11], v[8:9], 0, s[30:31]
	s_min_i32 s13, s13, s56
	s_mul_i32 s59, s16, s14
	v_lshl_add_u64 v[12:13], v[10:11], 0, s[30:31]
	s_add_i32 s13, s13, s59
	v_lshl_add_u64 v[14:15], v[12:13], 0, s[30:31]
	s_mul_i32 s42, s13, s17
	v_lshl_add_u64 v[16:17], v[14:15], 0, s[30:31]
	s_ashr_i32 s43, s42, 31
	v_lshl_add_u64 v[36:37], v[16:17], 0, s[30:31]
	v_lshl_add_u64 v[4:5], s[42:43], 2, v[4:5]
	v_lshl_add_u64 v[46:47], v[36:37], 0, s[30:31]
	global_load_dword v40, v[6:7], off
	global_load_dword v39, v[8:9], off
	global_load_dword v22, v[10:11], off
	global_load_dword v23, v[12:13], off
	global_load_dword v18, v[14:15], off
	global_load_dword v19, v[16:17], off
	global_load_dword v20, v[36:37], off
	global_load_dword v21, v[46:47], off
	v_lshl_add_u64 v[6:7], v[4:5], 0, s[30:31]
	v_lshl_add_u64 v[8:9], v[6:7], 0, s[30:31]
	v_lshl_add_u64 v[10:11], v[8:9], 0, s[30:31]
	v_lshl_add_u64 v[46:47], v[10:11], 0, s[30:31]
	v_lshl_add_u64 v[48:49], v[46:47], 0, s[30:31]
	v_lshl_add_u64 v[50:51], v[48:49], 0, s[30:31]
	v_lshl_add_u64 v[52:53], v[50:51], 0, s[30:31]
	global_load_dword v38, v[4:5], off
	global_load_dword v37, v[6:7], off
	global_load_dword v16, v[8:9], off
	global_load_dword v17, v[10:11], off
	global_load_dword v12, v[46:47], off
	global_load_dword v13, v[48:49], off
	global_load_dword v14, v[50:51], off
	global_load_dword v15, v[52:53], off
	s_cmpk_gt_u32 s12, 0x7f
	s_cselect_b64 s[44:45], -1, 0
	s_and_b64 vcc, exec, s[44:45]
	s_cbranch_vccz .LBB4_2
	v_cmp_lt_u32_e32 vcc, 8, v1
	v_min_u32_e32 v3, 17, v1
	s_nop 0
	v_cndmask_b32_e64 v1, 0, -9, vcc
	v_add3_u32 v1, v3, s54, v1
	v_max_i32_e32 v1, 0, v1
	v_min_i32_e32 v4, s56, v1
	v_cndmask_b32_e64 v1, 0, 8, vcc
	v_or_b32_e32 v1, s55, v1
	v_mad_u64_u32 v[4:5], s[12:13], v1, s16, v[4:5]
	v_mul_lo_u32 v1, v4, s17
	s_max_i32 s12, s24, 0
	v_add_u32_e32 v4, s12, v1
	v_mov_b32_e32 v171, s12
	s_load_dwordx2 s[12:13], s[0:1], 0x8
	s_cbranch_execz .LBB4_3
	s_branch .LBB4_4

.LBB5_63:
	s_load_dwordx8 s[40:47], s[0:1], 0x38
	s_load_dwordx2 s[8:9], s[0:1], 0x18
	s_load_dwordx2 s[6:7], s[0:1], 0x28
	s_bfe_u32 s10, s33, 0x20006
	s_waitcnt vmcnt(0)
	v_lshlrev_b64 v[34:35], 4, v[146:147]
	s_lshl_b32 s12, s10, 11
	s_waitcnt lgkmcnt(0)
	s_mov_b32 s13, 0
	v_add_u32_e32 v99, s12, v34
	s_mov_b32 s60, s8
	s_mov_b32 s61, s9
	global_load_dwordx4 v[100:103], v99, s[60:61] offset:16
	global_load_dwordx4 v[104:107], v99, s[60:61]
	s_add_u32 s60, s60, 0x2000
	s_addc_u32 s61, s61, 0
	global_load_dwordx4 v[108:111], v99, s[60:61] offset:16
	global_load_dwordx4 v[112:115], v99, s[60:61]
	s_add_u32 s60, s60, 0x2000
	s_addc_u32 s61, s61, 0
	global_load_dwordx4 v[116:119], v99, s[60:61] offset:16
	global_load_dwordx4 v[120:123], v99, s[60:61]
	s_add_u32 s60, s60, 0x2000
	s_addc_u32 s61, s61, 0
	global_load_dwordx4 v[124:127], v99, s[60:61] offset:16
	global_load_dwordx4 v[128:131], v99, s[60:61]
	s_add_u32 s60, s60, 0x2000
	s_addc_u32 s61, s61, 0
	global_load_dwordx4 v[136:139], v99, s[60:61] offset:16
	global_load_dwordx4 v[140:143], v99, s[60:61]
	s_add_u32 s60, s60, 0x2000
	s_addc_u32 s61, s61, 0
	global_load_dwordx4 v[156:159], v99, s[60:61] offset:16
	global_load_dwordx4 v[160:163], v99, s[60:61]
	s_add_u32 s60, s60, 0x2000
	s_addc_u32 s61, s61, 0
	global_load_dwordx4 v[164:167], v99, s[60:61] offset:16
	global_load_dwordx4 v[168:171], v99, s[60:61]
	s_add_u32 s60, s60, 0x2000
	s_addc_u32 s61, s61, 0
	global_load_dwordx4 v[172:175], v99, s[60:61] offset:16
	global_load_dwordx4 v[176:179], v99, s[60:61]
	s_add_u32 s60, s60, 0x2000
	s_addc_u32 s61, s61, 0
	global_load_dwordx4 v[180:183], v99, s[60:61] offset:16
	global_load_dwordx4 v[184:187], v99, s[60:61]
	s_add_u32 s60, s60, 0x2000
	s_addc_u32 s61, s61, 0
	global_load_dwordx4 v[188:191], v99, s[60:61] offset:16
	global_load_dwordx4 v[192:195], v99, s[60:61]
	s_add_u32 s60, s60, 0x2000
	s_addc_u32 s61, s61, 0
	global_load_dwordx4 v[196:199], v99, s[60:61] offset:16
	global_load_dwordx4 v[200:203], v99, s[60:61]
	s_add_u32 s60, s60, 0x2000
	s_addc_u32 s61, s61, 0
	global_load_dwordx4 v[204:207], v99, s[60:61] offset:16
	global_load_dwordx4 v[208:211], v99, s[60:61]
	s_add_u32 s60, s60, 0x2000
	s_addc_u32 s61, s61, 0
	global_load_dwordx4 v[212:215], v99, s[60:61] offset:16
	global_load_dwordx4 v[216:219], v99, s[60:61]
	s_add_u32 s60, s60, 0x2000
	s_addc_u32 s61, s61, 0
	global_load_dwordx4 v[220:223], v99, s[60:61] offset:16
	global_load_dwordx4 v[224:227], v99, s[60:61]
	s_add_u32 s60, s60, 0x2000
	s_addc_u32 s61, s61, 0
	global_load_dwordx4 v[228:231], v99, s[60:61] offset:16
	global_load_dwordx4 v[232:235], v99, s[60:61]
	s_add_u32 s60, s60, 0x2000
	s_addc_u32 s61, s61, 0
	global_load_dwordx4 v[236:239], v99, s[60:61] offset:16
	global_load_dwordx4 v[240:243], v99, s[60:61]
	s_barrier
	s_lshr_b32 s8, s33, 2
	s_and_b32 s8, s8, 0x3fffffc0
	s_movk_i32 s9, 0x110
	v_or_b32_e32 v38, s8, v150
	v_mul_lo_u32 v39, v38, s9
	v_add_u32_e32 v132, v152, v39
	v_add_u32_e32 v133, 0x2200, v132
	v_add_u32_e32 v144, 0x11000, v132
	v_add_u32_e32 v145, 0x11000, v133
	ds_read_b128 v[40:43], v132
	ds_read_b128 v[44:47], v132 offset:16
	ds_read_b128 v[48:51], v133
	ds_read_b128 v[52:55], v133 offset:16
	v_mov_b32_e32 v75, 0
	s_lshl_b32 s50, s5, 2
	s_mov_b32 s51, s13
	v_lshl_add_u64 v[76:77], s[6:7], 0, v[34:35]
	s_lshl_b64 s[6:7], s[50:51], 11
	v_mov_b32_e32 v82, 0xff7fc99e
	s_brev_b32 s14, 35
	v_mov_b32_e32 v84, 0xff7fc99e
	v_mov_b32_e32 v86, 0xff7fc99e
	v_mov_b32_e32 v87, 0xff7fc99e
	v_mov_b32_e32 v88, 0xff7fc99e
	v_mov_b32_e32 v90, 0xff7fc99e
	v_mov_b32_e32 v91, 0xff7fc99e
	v_mov_b32_e32 v92, 0xff7fc99e
	v_mov_b32_e32 v94, 0xff7fc99e
	v_mov_b32_e32 v95, 0xff7fc99e
	v_mov_b32_e32 v97, 0xff7fc99e
	v_mov_b32_e32 v80, v75
	v_mov_b32_e32 v81, v75
	v_mov_b32_e32 v83, 0xff7fc99e
	v_mov_b32_e32 v98, 0xff7fc99e
	v_mov_b32_e32 v93, 0xff7fc99e
	v_mov_b32_e32 v89, 0xff7fc99e
	v_mov_b32_e32 v85, 0xff7fc99e
	s_mov_b32 s15, 0
	ds_read_b128 v[56:59], v132 offset:64
	ds_read_b128 v[60:63], v132 offset:80
	ds_read_b128 v[64:67], v133 offset:64
	ds_read_b128 v[68:71], v133 offset:80
	s_waitcnt vmcnt(31) lgkmcnt(7)
	v_mfma_f32_32x32x16_f16 v[18:33], v[100:103], v[40:43], 0
	s_waitcnt lgkmcnt(5)
	v_mfma_f32_32x32x16_f16 v[2:17], v[100:103], v[48:51], 0
	s_waitcnt vmcnt(30) lgkmcnt(4)
	v_mfma_f32_32x32x16_f16 v[18:33], v[104:107], v[44:47], v[18:33]
	v_mfma_f32_32x32x16_f16 v[2:17], v[104:107], v[52:55], v[2:17]
	v_mfma_f32_32x32x16_f16 v[18:33], v[104:107], v[40:43], v[18:33]
	v_mfma_f32_32x32x16_f16 v[2:17], v[104:107], v[48:51], v[2:17]
	ds_read_b128 v[40:43], v132 offset:128
	ds_read_b128 v[44:47], v132 offset:144
	ds_read_b128 v[48:51], v133 offset:128
	ds_read_b128 v[52:55], v133 offset:144
	s_waitcnt vmcnt(29) lgkmcnt(7)
	v_mfma_f32_32x32x16_f16 v[18:33], v[108:111], v[56:59], v[18:33]
	s_waitcnt lgkmcnt(5)
	v_mfma_f32_32x32x16_f16 v[2:17], v[108:111], v[64:67], v[2:17]
	s_waitcnt vmcnt(28) lgkmcnt(4)
	v_mfma_f32_32x32x16_f16 v[18:33], v[112:115], v[60:63], v[18:33]
	v_mfma_f32_32x32x16_f16 v[2:17], v[112:115], v[68:71], v[2:17]
	v_mfma_f32_32x32x16_f16 v[18:33], v[112:115], v[56:59], v[18:33]
	v_mfma_f32_32x32x16_f16 v[2:17], v[112:115], v[64:67], v[2:17]
	ds_read_b128 v[56:59], v132 offset:192
	ds_read_b128 v[60:63], v132 offset:208
	ds_read_b128 v[64:67], v133 offset:192
	ds_read_b128 v[68:71], v133 offset:208
	s_waitcnt vmcnt(27) lgkmcnt(7)
	v_mfma_f32_32x32x16_f16 v[18:33], v[116:119], v[40:43], v[18:33]
	s_waitcnt lgkmcnt(5)
	v_mfma_f32_32x32x16_f16 v[2:17], v[116:119], v[48:51], v[2:17]
	s_waitcnt vmcnt(26) lgkmcnt(4)
	v_mfma_f32_32x32x16_f16 v[18:33], v[120:123], v[44:47], v[18:33]
	v_mfma_f32_32x32x16_f16 v[2:17], v[120:123], v[52:55], v[2:17]
	v_mfma_f32_32x32x16_f16 v[18:33], v[120:123], v[40:43], v[18:33]
	v_mfma_f32_32x32x16_f16 v[2:17], v[120:123], v[48:51], v[2:17]
	ds_read_b128 v[40:43], v132 offset:34816
	ds_read_b128 v[44:47], v132 offset:34832
	ds_read_b128 v[48:51], v133 offset:34816
	ds_read_b128 v[52:55], v133 offset:34832
	s_waitcnt vmcnt(25) lgkmcnt(7)
	v_mfma_f32_32x32x16_f16 v[18:33], v[124:127], v[56:59], v[18:33]
	s_waitcnt lgkmcnt(5)
	v_mfma_f32_32x32x16_f16 v[2:17], v[124:127], v[64:67], v[2:17]
	s_waitcnt vmcnt(24) lgkmcnt(4)
	v_mfma_f32_32x32x16_f16 v[18:33], v[128:131], v[60:63], v[18:33]
	v_mfma_f32_32x32x16_f16 v[2:17], v[128:131], v[68:71], v[2:17]
	v_mfma_f32_32x32x16_f16 v[18:33], v[128:131], v[56:59], v[18:33]
	v_mfma_f32_32x32x16_f16 v[2:17], v[128:131], v[64:67], v[2:17]
	ds_read_b128 v[56:59], v132 offset:34880
	ds_read_b128 v[60:63], v132 offset:34896
	ds_read_b128 v[64:67], v133 offset:34880
	ds_read_b128 v[68:71], v133 offset:34896
	s_waitcnt vmcnt(23) lgkmcnt(7)
	v_mfma_f32_32x32x16_f16 v[18:33], v[136:139], v[40:43], v[18:33]
	s_waitcnt lgkmcnt(5)
	v_mfma_f32_32x32x16_f16 v[2:17], v[136:139], v[48:51], v[2:17]
	s_waitcnt vmcnt(22) lgkmcnt(4)
	v_mfma_f32_32x32x16_f16 v[18:33], v[140:143], v[44:47], v[18:33]
	v_mfma_f32_32x32x16_f16 v[2:17], v[140:143], v[52:55], v[2:17]
	v_mfma_f32_32x32x16_f16 v[18:33], v[140:143], v[40:43], v[18:33]
	v_mfma_f32_32x32x16_f16 v[2:17], v[140:143], v[48:51], v[2:17]
	ds_read_b128 v[40:43], v132 offset:34944
	ds_read_b128 v[44:47], v132 offset:34960
	ds_read_b128 v[48:51], v133 offset:34944
	ds_read_b128 v[52:55], v133 offset:34960
	s_waitcnt vmcnt(21) lgkmcnt(7)
	v_mfma_f32_32x32x16_f16 v[18:33], v[156:159], v[56:59], v[18:33]
	s_waitcnt lgkmcnt(5)
	v_mfma_f32_32x32x16_f16 v[2:17], v[156:159], v[64:67], v[2:17]
	s_waitcnt vmcnt(20) lgkmcnt(4)
	v_mfma_f32_32x32x16_f16 v[18:33], v[160:163], v[60:63], v[18:33]
	v_mfma_f32_32x32x16_f16 v[2:17], v[160:163], v[68:71], v[2:17]
	v_mfma_f32_32x32x16_f16 v[18:33], v[160:163], v[56:59], v[18:33]
	v_mfma_f32_32x32x16_f16 v[2:17], v[160:163], v[64:67], v[2:17]
	ds_read_b128 v[56:59], v132 offset:35008
	ds_read_b128 v[60:63], v132 offset:35024
	ds_read_b128 v[64:67], v133 offset:35008
	ds_read_b128 v[68:71], v133 offset:35024
	s_waitcnt vmcnt(19) lgkmcnt(7)
	v_mfma_f32_32x32x16_f16 v[18:33], v[164:167], v[40:43], v[18:33]
	s_waitcnt lgkmcnt(5)
	v_mfma_f32_32x32x16_f16 v[2:17], v[164:167], v[48:51], v[2:17]
	s_waitcnt vmcnt(18) lgkmcnt(4)
	v_mfma_f32_32x32x16_f16 v[18:33], v[168:171], v[44:47], v[18:33]
	v_mfma_f32_32x32x16_f16 v[2:17], v[168:171], v[52:55], v[2:17]
	v_mfma_f32_32x32x16_f16 v[18:33], v[168:171], v[40:43], v[18:33]
	v_mfma_f32_32x32x16_f16 v[2:17], v[168:171], v[48:51], v[2:17]
	ds_read_b128 v[40:43], v144
	ds_read_b128 v[44:47], v144 offset:16
	ds_read_b128 v[48:51], v145
	ds_read_b128 v[52:55], v145 offset:16
	s_waitcnt vmcnt(17) lgkmcnt(7)
	v_mfma_f32_32x32x16_f16 v[18:33], v[172:175], v[56:59], v[18:33]
	s_waitcnt lgkmcnt(5)
	v_mfma_f32_32x32x16_f16 v[2:17], v[172:175], v[64:67], v[2:17]
	s_waitcnt vmcnt(16) lgkmcnt(4)
	v_mfma_f32_32x32x16_f16 v[18:33], v[176:179], v[60:63], v[18:33]
	v_mfma_f32_32x32x16_f16 v[2:17], v[176:179], v[68:71], v[2:17]
	v_mfma_f32_32x32x16_f16 v[18:33], v[176:179], v[56:59], v[18:33]
	v_mfma_f32_32x32x16_f16 v[2:17], v[176:179], v[64:67], v[2:17]
	ds_read_b128 v[56:59], v144 offset:64
	ds_read_b128 v[60:63], v144 offset:80
	ds_read_b128 v[64:67], v145 offset:64
	ds_read_b128 v[68:71], v145 offset:80
	s_waitcnt vmcnt(15) lgkmcnt(7)
	v_mfma_f32_32x32x16_f16 v[18:33], v[180:183], v[40:43], v[18:33]
	s_waitcnt lgkmcnt(5)
	v_mfma_f32_32x32x16_f16 v[2:17], v[180:183], v[48:51], v[2:17]
	s_waitcnt vmcnt(14) lgkmcnt(4)
	v_mfma_f32_32x32x16_f16 v[18:33], v[184:187], v[44:47], v[18:33]
	v_mfma_f32_32x32x16_f16 v[2:17], v[184:187], v[52:55], v[2:17]
	v_mfma_f32_32x32x16_f16 v[18:33], v[184:187], v[40:43], v[18:33]
	v_mfma_f32_32x32x16_f16 v[2:17], v[184:187], v[48:51], v[2:17]
	ds_read_b128 v[40:43], v144 offset:128
	ds_read_b128 v[44:47], v144 offset:144
	ds_read_b128 v[48:51], v145 offset:128
	ds_read_b128 v[52:55], v145 offset:144
	s_waitcnt vmcnt(13) lgkmcnt(7)
	v_mfma_f32_32x32x16_f16 v[18:33], v[188:191], v[56:59], v[18:33]
	s_waitcnt lgkmcnt(5)
	v_mfma_f32_32x32x16_f16 v[2:17], v[188:191], v[64:67], v[2:17]
	s_waitcnt vmcnt(12) lgkmcnt(4)
	v_mfma_f32_32x32x16_f16 v[18:33], v[192:195], v[60:63], v[18:33]
	v_mfma_f32_32x32x16_f16 v[2:17], v[192:195], v[68:71], v[2:17]
	v_mfma_f32_32x32x16_f16 v[18:33], v[192:195], v[56:59], v[18:33]
	v_mfma_f32_32x32x16_f16 v[2:17], v[192:195], v[64:67], v[2:17]
	ds_read_b128 v[56:59], v144 offset:192
	ds_read_b128 v[60:63], v144 offset:208
	ds_read_b128 v[64:67], v145 offset:192
	ds_read_b128 v[68:71], v145 offset:208
	s_waitcnt vmcnt(11) lgkmcnt(7)
	v_mfma_f32_32x32x16_f16 v[18:33], v[196:199], v[40:43], v[18:33]
	s_waitcnt lgkmcnt(5)
	v_mfma_f32_32x32x16_f16 v[2:17], v[196:199], v[48:51], v[2:17]
	s_waitcnt vmcnt(10) lgkmcnt(4)
	v_mfma_f32_32x32x16_f16 v[18:33], v[200:203], v[44:47], v[18:33]
	v_mfma_f32_32x32x16_f16 v[2:17], v[200:203], v[52:55], v[2:17]
	v_mfma_f32_32x32x16_f16 v[18:33], v[200:203], v[40:43], v[18:33]
	v_mfma_f32_32x32x16_f16 v[2:17], v[200:203], v[48:51], v[2:17]
	ds_read_b128 v[40:43], v144 offset:34816
	ds_read_b128 v[44:47], v144 offset:34832
	ds_read_b128 v[48:51], v145 offset:34816
	ds_read_b128 v[52:55], v145 offset:34832
	s_waitcnt vmcnt(9) lgkmcnt(7)
	v_mfma_f32_32x32x16_f16 v[18:33], v[204:207], v[56:59], v[18:33]
	s_waitcnt lgkmcnt(5)
	v_mfma_f32_32x32x16_f16 v[2:17], v[204:207], v[64:67], v[2:17]
	s_waitcnt vmcnt(8) lgkmcnt(4)
	v_mfma_f32_32x32x16_f16 v[18:33], v[208:211], v[60:63], v[18:33]
	v_mfma_f32_32x32x16_f16 v[2:17], v[208:211], v[68:71], v[2:17]
	v_mfma_f32_32x32x16_f16 v[18:33], v[208:211], v[56:59], v[18:33]
	v_mfma_f32_32x32x16_f16 v[2:17], v[208:211], v[64:67], v[2:17]
	ds_read_b128 v[56:59], v144 offset:34880
	ds_read_b128 v[60:63], v144 offset:34896
	ds_read_b128 v[64:67], v145 offset:34880
	ds_read_b128 v[68:71], v145 offset:34896
	s_waitcnt vmcnt(7) lgkmcnt(7)
	v_mfma_f32_32x32x16_f16 v[18:33], v[212:215], v[40:43], v[18:33]
	s_waitcnt lgkmcnt(5)
	v_mfma_f32_32x32x16_f16 v[2:17], v[212:215], v[48:51], v[2:17]
	s_waitcnt vmcnt(6) lgkmcnt(4)
	v_mfma_f32_32x32x16_f16 v[18:33], v[216:219], v[44:47], v[18:33]
	v_mfma_f32_32x32x16_f16 v[2:17], v[216:219], v[52:55], v[2:17]
	v_mfma_f32_32x32x16_f16 v[18:33], v[216:219], v[40:43], v[18:33]
	v_mfma_f32_32x32x16_f16 v[2:17], v[216:219], v[48:51], v[2:17]
	ds_read_b128 v[40:43], v144 offset:34944
	ds_read_b128 v[44:47], v144 offset:34960
	ds_read_b128 v[48:51], v145 offset:34944
	ds_read_b128 v[52:55], v145 offset:34960
	s_waitcnt vmcnt(5) lgkmcnt(7)
	v_mfma_f32_32x32x16_f16 v[18:33], v[220:223], v[56:59], v[18:33]
	s_waitcnt lgkmcnt(5)
	v_mfma_f32_32x32x16_f16 v[2:17], v[220:223], v[64:67], v[2:17]
	s_waitcnt vmcnt(4) lgkmcnt(4)
	v_mfma_f32_32x32x16_f16 v[18:33], v[224:227], v[60:63], v[18:33]
	v_mfma_f32_32x32x16_f16 v[2:17], v[224:227], v[68:71], v[2:17]
	v_mfma_f32_32x32x16_f16 v[18:33], v[224:227], v[56:59], v[18:33]
	v_mfma_f32_32x32x16_f16 v[2:17], v[224:227], v[64:67], v[2:17]
	ds_read_b128 v[56:59], v144 offset:35008
	ds_read_b128 v[60:63], v144 offset:35024
	ds_read_b128 v[64:67], v145 offset:35008
	ds_read_b128 v[68:71], v145 offset:35024
	s_waitcnt vmcnt(3) lgkmcnt(7)
	v_mfma_f32_32x32x16_f16 v[18:33], v[228:231], v[40:43], v[18:33]
	s_waitcnt lgkmcnt(5)
	v_mfma_f32_32x32x16_f16 v[2:17], v[228:231], v[48:51], v[2:17]
	s_waitcnt vmcnt(2) lgkmcnt(4)
	v_mfma_f32_32x32x16_f16 v[18:33], v[232:235], v[44:47], v[18:33]
	v_mfma_f32_32x32x16_f16 v[2:17], v[232:235], v[52:55], v[2:17]
	v_mfma_f32_32x32x16_f16 v[18:33], v[232:235], v[40:43], v[18:33]
	s_lshl_b32 s8, s10, 5
	v_or_b32_e32 v74, s8, v134
	s_waitcnt vmcnt(0)
	v_lshl_add_u64 v[36:37], v[74:75], 2, s[24:25]
	s_waitcnt lgkmcnt(0)
	s_barrier
	v_add_u32_e32 v74, s8, v134
	v_mfma_f32_32x32x16_f16 v[2:17], v[232:235], v[48:51], v[2:17]
	global_load_dwordx4 v[48:51], v[36:37], off
	v_lshl_add_u64 v[36:37], v[74:75], 2, s[24:25]
	global_load_dwordx4 v[52:55], v[36:37], off offset:32
	s_mov_b32 s8, 0x3a800000
	v_mov_b32_e32 v74, v75
	s_waitcnt vmcnt(3)
	v_mfma_f32_32x32x16_f16 v[18:33], v[236:239], v[56:59], v[18:33]
	s_waitcnt vmcnt(2)
	v_mfma_f32_32x32x16_f16 v[18:33], v[240:243], v[60:63], v[18:33]
	v_lshl_add_u32 v62, s10, 7, v135
	s_mov_b32 s10, 0x41800000
	v_mov_b32_e32 v135, v75
	v_lshl_add_u64 v[78:79], v[134:135], 2, s[22:23]
	v_mfma_f32_32x32x16_f16 v[2:17], v[236:239], v[64:67], v[2:17]
	v_mfma_f32_32x32x16_f16 v[18:33], v[240:243], v[56:59], v[18:33]
	global_load_dwordx4 v[56:59], v[36:37], off offset:64
	v_mfma_f32_32x32x16_f16 v[2:17], v[240:243], v[68:71], v[2:17]
	s_waitcnt vmcnt(2)
	s_nop 8
	v_fma_f32 v18, v18, s8, v48
	v_fma_f32 v19, v19, s8, v49
	v_fma_f32 v20, v20, s8, v50
	v_fma_f32 v21, v21, s8, v51
	v_pk_mul_f32 v[60:61], v[18:19], s[10:11] op_sel_hi:[1,0]
	v_pk_mul_f32 v[46:47], v[20:21], s[10:11] op_sel_hi:[1,0]
	v_cvt_pk_f16_f32 v60, v60, v61
	v_cvt_f32_f16_e32 v44, v60
	v_cvt_f32_f16_sdwa v45, v60 dst_sel:DWORD dst_unused:UNUSED_PAD src0_sel:WORD_1
	v_mfma_f32_32x32x16_f16 v[2:17], v[240:243], v[64:67], v[2:17]
	v_cvt_pk_f16_f32 v61, v46, v47
	v_cvt_f32_f16_e32 v46, v61
	v_cvt_f32_f16_sdwa v47, v61 dst_sel:DWORD dst_unused:UNUSED_PAD src0_sel:WORD_1
	v_fma_f32 v18, v18, s10, -v44
	v_fma_f32 v19, v19, s10, -v45
	s_movk_i32 s9, 0x210
	v_cvt_pk_f16_f32 v44, v18, v19
	v_pk_fma_f32 v[18:19], v[20:21], s[10:11], v[46:47] op_sel_hi:[1,0,1] neg_lo:[0,0,1] neg_hi:[0,0,1]
	s_nop 3
	v_pk_fma_f32 v[2:3], v[2:3], s[8:9], v[48:49] op_sel_hi:[1,0,1]
	v_cvt_pk_f16_f32 v45, v18, v19
	v_pk_mul_f32 v[18:19], v[2:3], s[10:11] op_sel_hi:[1,0]
	v_mul_lo_u32 v46, v38, s9
	v_cvt_pk_f16_f32 v38, v18, v19
	global_load_dwordx4 v[18:21], v[36:37], off offset:96
	v_pk_fma_f32 v[4:5], v[4:5], s[8:9], v[50:51] op_sel_hi:[1,0,1]
	v_cvt_f32_f16_e32 v40, v38
	v_pk_mul_f32 v[36:37], v[4:5], s[10:11] op_sel_hi:[1,0]
	v_cvt_f32_f16_sdwa v41, v38 dst_sel:DWORD dst_unused:UNUSED_PAD src0_sel:WORD_1
	v_cvt_pk_f16_f32 v39, v36, v37
	v_cvt_f32_f16_e32 v36, v39
	v_cvt_f32_f16_sdwa v37, v39 dst_sel:DWORD dst_unused:UNUSED_PAD src0_sel:WORD_1
	v_pk_fma_f32 v[2:3], v[2:3], s[10:11], v[40:41] op_sel_hi:[1,0,1] neg_lo:[0,0,1] neg_hi:[0,0,1]
	v_add_u32_e32 v40, 0x4200, v46
	v_cvt_pk_f16_f32 v2, v2, v3
	v_pk_fma_f32 v[4:5], v[4:5], s[10:11], v[36:37] op_sel_hi:[1,0,1] neg_lo:[0,0,1] neg_hi:[0,0,1]
	s_waitcnt vmcnt(2)
	v_pk_fma_f32 v[24:25], v[24:25], s[8:9], v[54:55] op_sel_hi:[1,0,1]
	v_cvt_pk_f16_f32 v3, v4, v5
	v_add_u32_e32 v4, v62, v40
	ds_write2_b64 v4, v[38:39], v[2:3] offset1:2
	v_pk_fma_f32 v[2:3], v[22:23], s[8:9], v[52:53] op_sel_hi:[1,0,1]
	v_pk_mul_f32 v[36:37], v[24:25], s[10:11] op_sel_hi:[1,0]
	v_pk_mul_f32 v[4:5], v[2:3], s[10:11] op_sel_hi:[1,0]
	v_pk_fma_f32 v[6:7], v[6:7], s[8:9], v[52:53] op_sel_hi:[1,0,1]
	v_cvt_pk_f16_f32 v4, v4, v5
	v_cvt_pk_f16_f32 v5, v36, v37
	v_cvt_f32_f16_e32 v22, v4
	v_cvt_f32_f16_sdwa v23, v4 dst_sel:DWORD dst_unused:UNUSED_PAD src0_sel:WORD_1
	v_cvt_f32_f16_e32 v36, v5
	v_cvt_f32_f16_sdwa v37, v5 dst_sel:DWORD dst_unused:UNUSED_PAD src0_sel:WORD_1
	v_pk_fma_f32 v[8:9], v[8:9], s[8:9], v[54:55] op_sel_hi:[1,0,1]
	v_pk_fma_f32 v[2:3], v[2:3], s[10:11], v[22:23] op_sel_hi:[1,0,1] neg_lo:[0,0,1] neg_hi:[0,0,1]
	v_add_u32_e32 v38, 32, v62
	v_pk_fma_f32 v[22:23], v[24:25], s[10:11], v[36:37] op_sel_hi:[1,0,1] neg_lo:[0,0,1] neg_hi:[0,0,1]
	v_cvt_pk_f16_f32 v2, v2, v3
	v_cvt_pk_f16_f32 v3, v22, v23
	v_pk_mul_f32 v[22:23], v[6:7], s[10:11] op_sel_hi:[1,0]
	v_pk_mul_f32 v[36:37], v[8:9], s[10:11] op_sel_hi:[1,0]
	v_cvt_pk_f16_f32 v22, v22, v23
	v_cvt_pk_f16_f32 v23, v36, v37
	v_cvt_f32_f16_e32 v24, v22
	v_cvt_f32_f16_sdwa v25, v22 dst_sel:DWORD dst_unused:UNUSED_PAD src0_sel:WORD_1
	v_cvt_f32_f16_e32 v36, v23
	v_cvt_f32_f16_sdwa v37, v23 dst_sel:DWORD dst_unused:UNUSED_PAD src0_sel:WORD_1
	v_add_u32_e32 v39, v38, v46
	ds_write2_b64 v39, v[4:5], v[2:3] offset1:2
	v_pk_fma_f32 v[2:3], v[6:7], s[10:11], v[24:25] op_sel_hi:[1,0,1] neg_lo:[0,0,1] neg_hi:[0,0,1]
	v_pk_fma_f32 v[4:5], v[8:9], s[10:11], v[36:37] op_sel_hi:[1,0,1] neg_lo:[0,0,1] neg_hi:[0,0,1]
	v_cvt_pk_f16_f32 v2, v2, v3
	v_cvt_pk_f16_f32 v3, v4, v5
	v_add_u32_e32 v4, v38, v40
	ds_write2_b64 v4, v[22:23], v[2:3] offset1:2
	v_add_u32_e32 v24, 64, v62
	v_add_u32_e32 v25, v24, v46
	v_add_u32_e32 v47, v62, v46
	ds_write2_b64 v47, v[60:61], v[44:45] offset1:2
	s_waitcnt vmcnt(1)
	v_pk_fma_f32 v[2:3], v[26:27], s[8:9], v[56:57] op_sel_hi:[1,0,1]
	v_pk_fma_f32 v[8:9], v[28:29], s[8:9], v[58:59] op_sel_hi:[1,0,1]
	v_pk_mul_f32 v[4:5], v[2:3], s[10:11] op_sel_hi:[1,0]
	v_pk_mul_f32 v[22:23], v[8:9], s[10:11] op_sel_hi:[1,0]
	v_cvt_pk_f16_f32 v4, v4, v5
	v_cvt_pk_f16_f32 v5, v22, v23
	v_cvt_f32_f16_e32 v6, v4
	v_cvt_f32_f16_sdwa v7, v4 dst_sel:DWORD dst_unused:UNUSED_PAD src0_sel:WORD_1
	v_cvt_f32_f16_e32 v22, v5
	v_cvt_f32_f16_sdwa v23, v5 dst_sel:DWORD dst_unused:UNUSED_PAD src0_sel:WORD_1
	v_pk_fma_f32 v[12:13], v[12:13], s[8:9], v[58:59] op_sel_hi:[1,0,1]
	v_pk_fma_f32 v[2:3], v[2:3], s[10:11], v[6:7] op_sel_hi:[1,0,1] neg_lo:[0,0,1] neg_hi:[0,0,1]
	v_mad_u32_u24 v96, v150, s9, v152
	v_pk_fma_f32 v[6:7], v[8:9], s[10:11], v[22:23] op_sel_hi:[1,0,1] neg_lo:[0,0,1] neg_hi:[0,0,1]
	v_cvt_pk_f16_f32 v2, v2, v3
	v_cvt_pk_f16_f32 v3, v6, v7
	v_pk_fma_f32 v[6:7], v[10:11], s[8:9], v[56:57] op_sel_hi:[1,0,1]
	v_pk_mul_f32 v[22:23], v[12:13], s[10:11] op_sel_hi:[1,0]
	v_pk_mul_f32 v[8:9], v[6:7], s[10:11] op_sel_hi:[1,0]
	ds_write2_b64 v25, v[4:5], v[2:3] offset1:2
	v_cvt_pk_f16_f32 v8, v8, v9
	v_cvt_pk_f16_f32 v9, v22, v23
	v_cvt_f32_f16_e32 v10, v8
	v_cvt_f32_f16_sdwa v11, v8 dst_sel:DWORD dst_unused:UNUSED_PAD src0_sel:WORD_1
	v_cvt_f32_f16_e32 v22, v9
	v_cvt_f32_f16_sdwa v23, v9 dst_sel:DWORD dst_unused:UNUSED_PAD src0_sel:WORD_1
	v_pk_fma_f32 v[2:3], v[6:7], s[10:11], v[10:11] op_sel_hi:[1,0,1] neg_lo:[0,0,1] neg_hi:[0,0,1]
	s_nop 0
	v_cvt_pk_f16_f32 v2, v2, v3
	v_pk_fma_f32 v[4:5], v[12:13], s[10:11], v[22:23] op_sel_hi:[1,0,1] neg_lo:[0,0,1] neg_hi:[0,0,1]
	s_waitcnt vmcnt(0)
	v_pk_fma_f32 v[12:13], v[16:17], s[8:9], v[20:21] op_sel_hi:[1,0,1]
	v_cvt_pk_f16_f32 v3, v4, v5
	v_add_u32_e32 v4, v24, v40
	ds_write2_b64 v4, v[8:9], v[2:3] offset1:2
	v_pk_fma_f32 v[2:3], v[30:31], s[8:9], v[18:19] op_sel_hi:[1,0,1]
	v_pk_fma_f32 v[8:9], v[32:33], s[8:9], v[20:21] op_sel_hi:[1,0,1]
	v_pk_mul_f32 v[4:5], v[2:3], s[10:11] op_sel_hi:[1,0]
	v_pk_mul_f32 v[10:11], v[8:9], s[10:11] op_sel_hi:[1,0]
	v_cvt_pk_f16_f32 v4, v4, v5
	v_cvt_pk_f16_f32 v5, v10, v11
	v_cvt_f32_f16_e32 v6, v4
	v_cvt_f32_f16_sdwa v7, v4 dst_sel:DWORD dst_unused:UNUSED_PAD src0_sel:WORD_1
	v_cvt_f32_f16_e32 v10, v5
	v_cvt_f32_f16_sdwa v11, v5 dst_sel:DWORD dst_unused:UNUSED_PAD src0_sel:WORD_1
	v_add_u32_e32 v22, 0x60, v62
	v_pk_fma_f32 v[2:3], v[2:3], s[10:11], v[6:7] op_sel_hi:[1,0,1] neg_lo:[0,0,1] neg_hi:[0,0,1]
	v_add_u32_e32 v23, v22, v46
	v_pk_fma_f32 v[6:7], v[8:9], s[10:11], v[10:11] op_sel_hi:[1,0,1] neg_lo:[0,0,1] neg_hi:[0,0,1]
	v_cvt_pk_f16_f32 v2, v2, v3
	v_cvt_pk_f16_f32 v3, v6, v7
	v_pk_fma_f32 v[6:7], v[14:15], s[8:9], v[18:19] op_sel_hi:[1,0,1]
	v_pk_mul_f32 v[14:15], v[12:13], s[10:11] op_sel_hi:[1,0]
	v_pk_mul_f32 v[8:9], v[6:7], s[10:11] op_sel_hi:[1,0]
	ds_write2_b64 v23, v[4:5], v[2:3] offset1:2
	v_cvt_pk_f16_f32 v8, v8, v9
	v_cvt_pk_f16_f32 v9, v14, v15
	v_cvt_f32_f16_e32 v10, v8
	v_cvt_f32_f16_sdwa v11, v8 dst_sel:DWORD dst_unused:UNUSED_PAD src0_sel:WORD_1
	v_cvt_f32_f16_e32 v14, v9
	v_cvt_f32_f16_sdwa v15, v9 dst_sel:DWORD dst_unused:UNUSED_PAD src0_sel:WORD_1
	v_pk_fma_f32 v[2:3], v[6:7], s[10:11], v[10:11] op_sel_hi:[1,0,1] neg_lo:[0,0,1] neg_hi:[0,0,1]
	s_nop 0
	v_cvt_pk_f16_f32 v2, v2, v3
	v_pk_fma_f32 v[4:5], v[12:13], s[10:11], v[14:15] op_sel_hi:[1,0,1] neg_lo:[0,0,1] neg_hi:[0,0,1]
	s_nop 0
	v_cvt_pk_f16_f32 v3, v4, v5
	v_add_u32_e32 v4, v22, v40
	ds_write2_b64 v4, v[8:9], v[2:3] offset1:2
	v_lshl_add_u64 v[2:3], v[76:77], 0, s[6:7]
	s_waitcnt lgkmcnt(0)
	s_barrier
	global_load_dwordx4 v[66:69], v[2:3], off
	global_load_dwordx4 v[70:73], v[2:3], off offset:16
	s_cmp_lt_u32 s5, 4
	s_cbranch_scc1 .Lvq_nosleep
	s_sleep 24
.Lvq_nosleep:
.LBB5_64:
	s_or_b32 s6, s15, s50
	s_lshl_b32 s12, s6, 5
	s_add_i32 s8, s6, 32
	s_mov_b32 s9, s13
	v_lshl_add_u64 v[10:11], s[12:13], 2, v[78:79]
	s_lshl_b64 s[8:9], s[8:9], 11
	global_load_dwordx4 v[2:5], v[10:11], off offset:64
	global_load_dwordx4 v[6:9], v[10:11], off offset:96
	global_load_dwordx4 v[16:19], v[10:11], off
	global_load_dwordx4 v[20:23], v[10:11], off offset:32
	v_lshl_add_u64 v[10:11], v[76:77], 0, s[8:9]
	global_load_dwordx4 v[100:103], v[10:11], off
	global_load_dwordx4 v[104:107], v[10:11], off offset:16
	ds_read_b128 v[34:37], v96
	ds_read_b128 v[38:41], v96 offset:16
	ds_read_b128 v[50:53], v96 offset:16896
	ds_read_b128 v[54:57], v96 offset:16912
	ds_read_b128 v[108:111], v96 offset:33792
	ds_read_b128 v[112:115], v96 offset:33808
	ds_read_b128 v[116:119], v96 offset:50688
	ds_read_b128 v[120:123], v96 offset:50704
	ds_read_b128 v[124:127], v96 offset:64
	ds_read_b128 v[128:131], v96 offset:80
	ds_read_b128 v[136:139], v96 offset:16960
	ds_read_b128 v[140:143], v96 offset:16976
	ds_read_b128 v[144:147], v96 offset:33856
	ds_read_b128 v[152:155], v96 offset:33872
	ds_read_b128 v[156:159], v96 offset:50752
	ds_read_b128 v[160:163], v96 offset:50768
	s_waitcnt vmcnt(5)
	v_pk_mul_f32 v[10:11], v[2:3], s[14:15] op_sel_hi:[1,0]
	s_waitcnt vmcnt(4)
	v_pk_mul_f32 v[14:15], v[6:7], s[14:15] op_sel_hi:[1,0]
	s_waitcnt vmcnt(3)
	v_pk_mul_f32 v[2:3], v[16:17], s[14:15] op_sel_hi:[1,0]
	s_waitcnt vmcnt(2)
	v_pk_mul_f32 v[6:7], v[20:21], s[14:15] op_sel_hi:[1,0]
	v_pk_mul_f32 v[16:17], v[8:9], s[14:15] op_sel_hi:[1,0]
	v_pk_mul_f32 v[12:13], v[4:5], s[14:15] op_sel_hi:[1,0]
	v_pk_mul_f32 v[8:9], v[22:23], s[14:15] op_sel_hi:[1,0]
	v_pk_mul_f32 v[4:5], v[18:19], s[14:15] op_sel_hi:[1,0]
	s_waitcnt lgkmcnt(14)
	s_nop 0
	v_mfma_f32_32x32x16_f16 v[18:33], v[70:73], v[34:37], v[2:17]
	v_mfma_f32_32x32x16_f16 v[18:33], v[66:69], v[38:41], v[18:33]
	v_mfma_f32_32x32x16_f16 v[18:33], v[66:69], v[34:37], v[18:33]
	s_waitcnt lgkmcnt(13)
	v_mfma_f32_32x32x16_f16 v[34:49], v[70:73], v[50:53], v[2:17]
	s_waitcnt lgkmcnt(12)
	v_mfma_f32_32x32x16_f16 v[34:49], v[66:69], v[54:57], v[34:49]
	v_mfma_f32_32x32x16_f16 v[34:49], v[66:69], v[50:53], v[34:49]
	s_waitcnt lgkmcnt(11)
	v_mfma_f32_32x32x16_f16 v[50:65], v[70:73], v[108:111], v[2:17]
	s_waitcnt lgkmcnt(9)
	v_mfma_f32_32x32x16_f16 v[2:17], v[70:73], v[116:119], v[2:17]
	v_mfma_f32_32x32x16_f16 v[50:65], v[66:69], v[112:115], v[50:65]
	s_waitcnt lgkmcnt(8)
	v_mfma_f32_32x32x16_f16 v[2:17], v[66:69], v[120:123], v[2:17]
	v_mfma_f32_32x32x16_f16 v[50:65], v[66:69], v[108:111], v[50:65]
	v_mfma_f32_32x32x16_f16 v[2:17], v[66:69], v[116:119], v[2:17]
	s_add_i32 s8, s6, 64
	s_mov_b32 s9, s13
	s_lshl_b64 s[8:9], s[8:9], 11
	v_lshl_add_u64 v[70:71], v[76:77], 0, s[8:9]
	global_load_dwordx4 v[66:69], v[70:71], off
	s_nop 0
	global_load_dwordx4 v[70:73], v[70:71], off offset:16
	ds_read_b128 v[108:111], v96 offset:128
	ds_read_b128 v[112:115], v96 offset:144
	ds_read_b128 v[116:119], v96 offset:17024
	ds_read_b128 v[120:123], v96 offset:17040
	ds_read_b128 v[164:167], v96 offset:33920
	ds_read_b128 v[168:171], v96 offset:33936
	ds_read_b128 v[172:175], v96 offset:50816
	ds_read_b128 v[176:179], v96 offset:50832
	s_waitcnt vmcnt(2) lgkmcnt(14)
	v_mfma_f32_32x32x16_f16 v[18:33], v[104:107], v[124:127], v[18:33]
	s_waitcnt lgkmcnt(13)
	v_mfma_f32_32x32x16_f16 v[34:49], v[104:107], v[136:139], v[34:49]
	s_waitcnt lgkmcnt(11)
	v_mfma_f32_32x32x16_f16 v[50:65], v[104:107], v[144:147], v[50:65]
	s_waitcnt lgkmcnt(9)
	v_mfma_f32_32x32x16_f16 v[2:17], v[104:107], v[156:159], v[2:17]
	v_mfma_f32_32x32x16_f16 v[18:33], v[100:103], v[128:131], v[18:33]
	v_mfma_f32_32x32x16_f16 v[34:49], v[100:103], v[140:143], v[34:49]
	v_mfma_f32_32x32x16_f16 v[50:65], v[100:103], v[152:155], v[50:65]
	s_waitcnt lgkmcnt(8)
	v_mfma_f32_32x32x16_f16 v[2:17], v[100:103], v[160:163], v[2:17]
	v_mfma_f32_32x32x16_f16 v[18:33], v[100:103], v[124:127], v[18:33]
	v_mfma_f32_32x32x16_f16 v[34:49], v[100:103], v[136:139], v[34:49]
	v_mfma_f32_32x32x16_f16 v[50:65], v[100:103], v[144:147], v[50:65]
	v_mfma_f32_32x32x16_f16 v[2:17], v[100:103], v[156:159], v[2:17]
	s_add_i32 s8, s6, 0x60
	s_mov_b32 s9, s13
	s_lshl_b64 s[8:9], s[8:9], 11
	v_lshl_add_u64 v[104:105], v[76:77], 0, s[8:9]
	global_load_dwordx4 v[100:103], v[104:105], off
	s_nop 0
	global_load_dwordx4 v[104:107], v[104:105], off offset:16
	ds_read_b128 v[124:127], v96 offset:192
	ds_read_b128 v[128:131], v96 offset:208
	ds_read_b128 v[136:139], v96 offset:17088
	ds_read_b128 v[140:143], v96 offset:17104
	ds_read_b128 v[144:147], v96 offset:33984
	ds_read_b128 v[152:155], v96 offset:34000
	ds_read_b128 v[156:159], v96 offset:50880
	ds_read_b128 v[160:163], v96 offset:50896
	s_waitcnt vmcnt(2) lgkmcnt(14)
	v_mfma_f32_32x32x16_f16 v[18:33], v[70:73], v[108:111], v[18:33]
	s_waitcnt lgkmcnt(13)
	v_mfma_f32_32x32x16_f16 v[34:49], v[70:73], v[116:119], v[34:49]
	s_waitcnt lgkmcnt(11)
	v_mfma_f32_32x32x16_f16 v[50:65], v[70:73], v[164:167], v[50:65]
	s_waitcnt lgkmcnt(9)
	v_mfma_f32_32x32x16_f16 v[2:17], v[70:73], v[172:175], v[2:17]
	v_mfma_f32_32x32x16_f16 v[18:33], v[66:69], v[112:115], v[18:33]
	v_mfma_f32_32x32x16_f16 v[34:49], v[66:69], v[120:123], v[34:49]
	v_mfma_f32_32x32x16_f16 v[50:65], v[66:69], v[168:171], v[50:65]
	s_waitcnt lgkmcnt(8)
	v_mfma_f32_32x32x16_f16 v[2:17], v[66:69], v[176:179], v[2:17]
	v_mfma_f32_32x32x16_f16 v[18:33], v[66:69], v[108:111], v[18:33]
	v_mfma_f32_32x32x16_f16 v[34:49], v[66:69], v[116:119], v[34:49]
	v_mfma_f32_32x32x16_f16 v[50:65], v[66:69], v[164:167], v[50:65]
	v_mfma_f32_32x32x16_f16 v[2:17], v[66:69], v[172:175], v[2:17]
	s_add_i32 s8, s6, 0x80
	s_mov_b32 s9, s13
	s_lshl_b64 s[8:9], s[8:9], 11
	v_lshl_add_u64 v[70:71], v[76:77], 0, s[8:9]
	global_load_dwordx4 v[66:69], v[70:71], off
	s_nop 0
	global_load_dwordx4 v[70:73], v[70:71], off offset:16
	ds_read_b128 v[108:111], v96 offset:256
	ds_read_b128 v[112:115], v96 offset:272
	ds_read_b128 v[116:119], v96 offset:17152
	ds_read_b128 v[120:123], v96 offset:17168
	ds_read_b128 v[164:167], v96 offset:34048
	ds_read_b128 v[168:171], v96 offset:34064
	ds_read_b128 v[172:175], v96 offset:50944
	ds_read_b128 v[176:179], v96 offset:50960
	s_waitcnt vmcnt(2) lgkmcnt(14)
	v_mfma_f32_32x32x16_f16 v[18:33], v[104:107], v[124:127], v[18:33]
	s_waitcnt lgkmcnt(13)
	v_mfma_f32_32x32x16_f16 v[34:49], v[104:107], v[136:139], v[34:49]
	s_waitcnt lgkmcnt(11)
	v_mfma_f32_32x32x16_f16 v[50:65], v[104:107], v[144:147], v[50:65]
	s_waitcnt lgkmcnt(9)
	v_mfma_f32_32x32x16_f16 v[2:17], v[104:107], v[156:159], v[2:17]
	v_mfma_f32_32x32x16_f16 v[18:33], v[100:103], v[128:131], v[18:33]
	v_mfma_f32_32x32x16_f16 v[34:49], v[100:103], v[140:143], v[34:49]
	v_mfma_f32_32x32x16_f16 v[50:65], v[100:103], v[152:155], v[50:65]
	s_waitcnt lgkmcnt(8)
	v_mfma_f32_32x32x16_f16 v[2:17], v[100:103], v[160:163], v[2:17]
	v_mfma_f32_32x32x16_f16 v[18:33], v[100:103], v[124:127], v[18:33]
	v_mfma_f32_32x32x16_f16 v[34:49], v[100:103], v[136:139], v[34:49]
	v_mfma_f32_32x32x16_f16 v[50:65], v[100:103], v[144:147], v[50:65]
	v_mfma_f32_32x32x16_f16 v[2:17], v[100:103], v[156:159], v[2:17]
	s_add_i32 s8, s6, 0xa0
	s_mov_b32 s9, s13
	s_lshl_b64 s[8:9], s[8:9], 11
	v_lshl_add_u64 v[104:105], v[76:77], 0, s[8:9]
	global_load_dwordx4 v[100:103], v[104:105], off
	s_nop 0
	global_load_dwordx4 v[104:107], v[104:105], off offset:16
	ds_read_b128 v[124:127], v96 offset:320
	ds_read_b128 v[128:131], v96 offset:336
	ds_read_b128 v[136:139], v96 offset:17216
	ds_read_b128 v[140:143], v96 offset:17232
	ds_read_b128 v[144:147], v96 offset:34112
	ds_read_b128 v[152:155], v96 offset:34128
	ds_read_b128 v[156:159], v96 offset:51008
	ds_read_b128 v[160:163], v96 offset:51024
	s_waitcnt vmcnt(2) lgkmcnt(14)
	v_mfma_f32_32x32x16_f16 v[18:33], v[70:73], v[108:111], v[18:33]
	s_waitcnt lgkmcnt(13)
	v_mfma_f32_32x32x16_f16 v[34:49], v[70:73], v[116:119], v[34:49]
	s_waitcnt lgkmcnt(11)
	v_mfma_f32_32x32x16_f16 v[50:65], v[70:73], v[164:167], v[50:65]
	s_waitcnt lgkmcnt(9)
	v_mfma_f32_32x32x16_f16 v[2:17], v[70:73], v[172:175], v[2:17]
	v_mfma_f32_32x32x16_f16 v[18:33], v[66:69], v[112:115], v[18:33]
	v_mfma_f32_32x32x16_f16 v[34:49], v[66:69], v[120:123], v[34:49]
	v_mfma_f32_32x32x16_f16 v[50:65], v[66:69], v[168:171], v[50:65]
	s_waitcnt lgkmcnt(8)
	v_mfma_f32_32x32x16_f16 v[2:17], v[66:69], v[176:179], v[2:17]
	v_mfma_f32_32x32x16_f16 v[18:33], v[66:69], v[108:111], v[18:33]
	v_mfma_f32_32x32x16_f16 v[34:49], v[66:69], v[116:119], v[34:49]
	v_mfma_f32_32x32x16_f16 v[50:65], v[66:69], v[164:167], v[50:65]
	v_mfma_f32_32x32x16_f16 v[2:17], v[66:69], v[172:175], v[2:17]
	s_add_i32 s8, s6, 0xc0
	s_mov_b32 s9, s13
	s_lshl_b64 s[8:9], s[8:9], 11
	v_lshl_add_u64 v[70:71], v[76:77], 0, s[8:9]
	global_load_dwordx4 v[66:69], v[70:71], off
	s_nop 0
	global_load_dwordx4 v[70:73], v[70:71], off offset:16
	ds_read_b128 v[108:111], v96 offset:384
	ds_read_b128 v[112:115], v96 offset:400
	ds_read_b128 v[116:119], v96 offset:17280
	ds_read_b128 v[120:123], v96 offset:17296
	ds_read_b128 v[164:167], v96 offset:34176
	ds_read_b128 v[168:171], v96 offset:34192
	ds_read_b128 v[172:175], v96 offset:51072
	ds_read_b128 v[176:179], v96 offset:51088
	s_waitcnt vmcnt(2) lgkmcnt(14)
	v_mfma_f32_32x32x16_f16 v[18:33], v[104:107], v[124:127], v[18:33]
	s_waitcnt lgkmcnt(13)
	v_mfma_f32_32x32x16_f16 v[34:49], v[104:107], v[136:139], v[34:49]
	s_waitcnt lgkmcnt(11)
	v_mfma_f32_32x32x16_f16 v[50:65], v[104:107], v[144:147], v[50:65]
	s_waitcnt lgkmcnt(9)
	v_mfma_f32_32x32x16_f16 v[2:17], v[104:107], v[156:159], v[2:17]
	v_mfma_f32_32x32x16_f16 v[18:33], v[100:103], v[128:131], v[18:33]
	v_mfma_f32_32x32x16_f16 v[34:49], v[100:103], v[140:143], v[34:49]
	v_mfma_f32_32x32x16_f16 v[50:65], v[100:103], v[152:155], v[50:65]
	s_waitcnt lgkmcnt(8)
	v_mfma_f32_32x32x16_f16 v[2:17], v[100:103], v[160:163], v[2:17]
	v_mfma_f32_32x32x16_f16 v[18:33], v[100:103], v[124:127], v[18:33]
	v_mfma_f32_32x32x16_f16 v[34:49], v[100:103], v[136:139], v[34:49]
	v_mfma_f32_32x32x16_f16 v[50:65], v[100:103], v[144:147], v[50:65]
	v_mfma_f32_32x32x16_f16 v[2:17], v[100:103], v[156:159], v[2:17]
	s_add_i32 s8, s6, 0xe0
	s_mov_b32 s9, s13
	s_lshl_b64 s[8:9], s[8:9], 11
	v_lshl_add_u64 v[104:105], v[76:77], 0, s[8:9]
	global_load_dwordx4 v[100:103], v[104:105], off
	s_nop 0
	global_load_dwordx4 v[104:107], v[104:105], off offset:16
	ds_read_b128 v[124:127], v96 offset:448
	ds_read_b128 v[128:131], v96 offset:464
	ds_read_b128 v[136:139], v96 offset:17344
	ds_read_b128 v[140:143], v96 offset:17360
	ds_read_b128 v[144:147], v96 offset:34240
	ds_read_b128 v[152:155], v96 offset:34256
	ds_read_b128 v[156:159], v96 offset:51136
	ds_read_b128 v[160:163], v96 offset:51152
	s_waitcnt vmcnt(2) lgkmcnt(14)
	v_mfma_f32_32x32x16_f16 v[18:33], v[70:73], v[108:111], v[18:33]
	s_waitcnt lgkmcnt(13)
	v_mfma_f32_32x32x16_f16 v[34:49], v[70:73], v[116:119], v[34:49]
	s_waitcnt lgkmcnt(11)
	v_mfma_f32_32x32x16_f16 v[50:65], v[70:73], v[164:167], v[50:65]
	s_waitcnt lgkmcnt(9)
	v_mfma_f32_32x32x16_f16 v[2:17], v[70:73], v[172:175], v[2:17]
	v_mfma_f32_32x32x16_f16 v[18:33], v[66:69], v[112:115], v[18:33]
	v_mfma_f32_32x32x16_f16 v[34:49], v[66:69], v[120:123], v[34:49]
	v_mfma_f32_32x32x16_f16 v[50:65], v[66:69], v[168:171], v[50:65]
	s_waitcnt lgkmcnt(8)
	v_mfma_f32_32x32x16_f16 v[2:17], v[66:69], v[176:179], v[2:17]
	v_mfma_f32_32x32x16_f16 v[18:33], v[66:69], v[108:111], v[18:33]
	v_mfma_f32_32x32x16_f16 v[34:49], v[66:69], v[116:119], v[34:49]
	v_mfma_f32_32x32x16_f16 v[50:65], v[66:69], v[164:167], v[50:65]
	v_mfma_f32_32x32x16_f16 v[2:17], v[66:69], v[172:175], v[2:17]
	s_waitcnt vmcnt(0) lgkmcnt(7)
	v_mfma_f32_32x32x16_f16 v[18:33], v[104:107], v[124:127], v[18:33]
	s_waitcnt lgkmcnt(5)
	v_mfma_f32_32x32x16_f16 v[34:49], v[104:107], v[136:139], v[34:49]
	s_waitcnt lgkmcnt(3)
	v_mfma_f32_32x32x16_f16 v[50:65], v[104:107], v[144:147], v[50:65]
	s_waitcnt lgkmcnt(1)
	v_mfma_f32_32x32x16_f16 v[2:17], v[104:107], v[156:159], v[2:17]
	v_mfma_f32_32x32x16_f16 v[18:33], v[100:103], v[128:131], v[18:33]
	v_mfma_f32_32x32x16_f16 v[34:49], v[100:103], v[140:143], v[34:49]
	v_mfma_f32_32x32x16_f16 v[50:65], v[100:103], v[152:155], v[50:65]
	s_waitcnt lgkmcnt(0)
	v_mfma_f32_32x32x16_f16 v[2:17], v[100:103], v[160:163], v[2:17]
	v_mfma_f32_32x32x16_f16 v[18:33], v[100:103], v[124:127], v[18:33]
	v_mfma_f32_32x32x16_f16 v[34:49], v[100:103], v[136:139], v[34:49]
	v_mfma_f32_32x32x16_f16 v[50:65], v[100:103], v[144:147], v[50:65]
	v_mfma_f32_32x32x16_f16 v[2:17], v[100:103], v[156:159], v[2:17]
	s_add_i32 s6, s6, 1
	s_mov_b32 s7, s13
	s_nop 6
	v_max_f32_e32 v25, v25, v25
	v_max_f32_e32 v70, v24, v24
	v_max_f32_e32 v41, v41, v41
	v_max_f32_e32 v71, v40, v40
	s_lshl_b64 s[6:7], s[6:7], 11
	v_max_f32_e32 v21, v21, v21
	v_max_f32_e32 v66, v20, v20
	v_max_f32_e32 v37, v37, v37
	v_max_f32_e32 v67, v36, v36
	v_max_f32_e32 v53, v53, v53
	v_max_f32_e32 v68, v52, v52
	v_max_f32_e32 v5, v5, v5
	v_max_f32_e32 v69, v4, v4
	v_max_f32_e32 v57, v57, v57
	v_max_f32_e32 v72, v56, v56
	v_max_f32_e32 v9, v9, v9
	v_max_f32_e32 v73, v8, v8
	v_max_f32_e32 v25, v70, v25
	v_max_f32_e32 v41, v71, v41
	v_lshl_add_u64 v[70:71], v[76:77], 0, s[6:7]
	v_max_f32_e32 v21, v66, v21
	v_max_f32_e32 v37, v67, v37
	v_max_f32_e32 v53, v68, v53
	v_max_f32_e32 v5, v69, v5
	v_max_f32_e32 v57, v72, v57
	v_max_f32_e32 v9, v73, v9
	global_load_dwordx4 v[66:69], v[70:71], off
	s_nop 0
	global_load_dwordx4 v[70:73], v[70:71], off offset:16
	v_max3_f32 v21, v18, v19, v21
	v_max3_f32 v37, v34, v35, v37
	v_max3_f32 v53, v50, v51, v53
	v_max3_f32 v5, v2, v3, v5
	v_cmp_gt_f32_e32 vcc, v21, v98
	v_cmp_gt_f32_e64 s[6:7], v37, v93
	v_cmp_gt_f32_e64 s[8:9], v53, v89
	v_cmp_gt_f32_e64 s[10:11], v5, v85
	v_or_b32_e32 v99, s12, v134
	v_max_f32_e32 v29, v29, v29
	v_max_f32_e32 v100, v28, v28
	v_max_f32_e32 v45, v45, v45
	v_max_f32_e32 v101, v44, v44
	v_max_f32_e32 v61, v61, v61
	v_max_f32_e32 v102, v60, v60
	v_max_f32_e32 v13, v13, v13
	v_max_f32_e32 v103, v12, v12
	v_max3_f32 v25, v22, v23, v25
	v_max3_f32 v41, v38, v39, v41
	v_max3_f32 v57, v54, v55, v57
	v_max3_f32 v9, v6, v7, v9
	v_cndmask_b32_e32 v21, v98, v21, vcc
	v_cndmask_b32_e64 v37, v93, v37, s[6:7]
	v_cndmask_b32_e64 v53, v89, v53, s[8:9]
	v_cndmask_b32_e64 v5, v85, v5, s[10:11]
	v_max_f32_e32 v29, v100, v29
	v_max_f32_e32 v45, v101, v45
	v_max_f32_e32 v61, v102, v61
	v_max_f32_e32 v13, v103, v13
	v_cndmask_b32_e32 v81, v81, v99, vcc
	v_cndmask_b32_e32 v18, v97, v18, vcc
	v_cndmask_b32_e32 v19, v95, v19, vcc
	v_cndmask_b32_e32 v20, v94, v20, vcc
	v_cndmask_b32_e64 v80, v80, v99, s[6:7]
	v_cndmask_b32_e64 v34, v92, v34, s[6:7]
	v_cndmask_b32_e64 v35, v91, v35, s[6:7]
	v_cndmask_b32_e64 v36, v90, v36, s[6:7]
	v_cndmask_b32_e64 v74, v74, v99, s[8:9]
	v_cndmask_b32_e64 v50, v88, v50, s[8:9]
	v_cndmask_b32_e64 v51, v87, v51, s[8:9]
	v_cndmask_b32_e64 v52, v86, v52, s[8:9]
	v_cndmask_b32_e64 v75, v75, v99, s[10:11]
	v_cndmask_b32_e64 v2, v84, v2, s[10:11]
	v_cndmask_b32_e64 v3, v82, v3, s[10:11]
	v_cndmask_b32_e64 v4, v83, v4, s[10:11]
	v_cmp_gt_f32_e32 vcc, v25, v21
	v_cmp_gt_f32_e64 s[6:7], v41, v37
	v_cmp_gt_f32_e64 s[8:9], v57, v53
	v_cmp_gt_f32_e64 s[10:11], v9, v5
	v_max_f32_e32 v33, v33, v33
	v_max_f32_e32 v104, v32, v32
	v_max_f32_e32 v49, v49, v49
	v_max_f32_e32 v105, v48, v48
	v_max_f32_e32 v65, v65, v65
	v_max_f32_e32 v106, v64, v64
	v_max_f32_e32 v17, v17, v17
	v_max_f32_e32 v107, v16, v16
	v_add_u32_e32 v108, 8, v99
	v_max3_f32 v29, v26, v27, v29
	v_max3_f32 v45, v42, v43, v45
	v_max3_f32 v61, v58, v59, v61
	v_max3_f32 v13, v10, v11, v13
	v_cndmask_b32_e32 v21, v21, v25, vcc
	v_cndmask_b32_e64 v25, v37, v41, s[6:7]
	v_cndmask_b32_e64 v37, v53, v57, s[8:9]
	v_cndmask_b32_e64 v5, v5, v9, s[10:11]
	v_max_f32_e32 v33, v104, v33
	v_max_f32_e32 v49, v105, v49
	v_max_f32_e32 v65, v106, v65
	v_max_f32_e32 v17, v107, v17
	v_cndmask_b32_e32 v9, v81, v108, vcc
	v_cndmask_b32_e32 v18, v18, v22, vcc
	v_cndmask_b32_e32 v19, v19, v23, vcc
	v_cndmask_b32_e32 v20, v20, v24, vcc
	v_cndmask_b32_e64 v22, v80, v108, s[6:7]
	v_cndmask_b32_e64 v23, v34, v38, s[6:7]
	v_cndmask_b32_e64 v24, v35, v39, s[6:7]
	v_cndmask_b32_e64 v34, v36, v40, s[6:7]
	v_cndmask_b32_e64 v35, v74, v108, s[8:9]
	v_cndmask_b32_e64 v36, v50, v54, s[8:9]
	v_cndmask_b32_e64 v38, v51, v55, s[8:9]
	v_cndmask_b32_e64 v39, v52, v56, s[8:9]
	v_cndmask_b32_e64 v40, v75, v108, s[10:11]
	v_cndmask_b32_e64 v2, v2, v6, s[10:11]
	v_cndmask_b32_e64 v3, v3, v7, s[10:11]
	v_cndmask_b32_e64 v4, v4, v8, s[10:11]
	v_cmp_gt_f32_e32 vcc, v29, v21
	v_cmp_gt_f32_e64 s[6:7], v45, v25
	v_cmp_gt_f32_e64 s[8:9], v61, v37
	v_cmp_gt_f32_e64 s[10:11], v13, v5
	v_add_u32_e32 v109, 16, v99
	v_max3_f32 v33, v30, v31, v33
	v_max3_f32 v49, v46, v47, v49
	v_max3_f32 v65, v62, v63, v65
	v_max3_f32 v17, v14, v15, v17
	v_cndmask_b32_e32 v6, v21, v29, vcc
	v_cndmask_b32_e64 v7, v25, v45, s[6:7]
	v_cndmask_b32_e64 v8, v37, v61, s[8:9]
	v_cndmask_b32_e64 v5, v5, v13, s[10:11]
	s_add_i32 s15, s15, 1
	v_add_u32_e32 v100, 24, v99
	v_cndmask_b32_e32 v9, v9, v109, vcc
	v_cndmask_b32_e32 v13, v18, v26, vcc
	v_cndmask_b32_e32 v18, v19, v27, vcc
	v_cndmask_b32_e32 v19, v20, v28, vcc
	v_cndmask_b32_e64 v20, v22, v109, s[6:7]
	v_cndmask_b32_e64 v21, v23, v42, s[6:7]
	v_cndmask_b32_e64 v22, v24, v43, s[6:7]
	v_cndmask_b32_e64 v23, v34, v44, s[6:7]
	v_cndmask_b32_e64 v24, v35, v109, s[8:9]
	v_cndmask_b32_e64 v25, v36, v58, s[8:9]
	v_cndmask_b32_e64 v26, v38, v59, s[8:9]
	v_cndmask_b32_e64 v27, v39, v60, s[8:9]
	v_cndmask_b32_e64 v28, v40, v109, s[10:11]
	v_cndmask_b32_e64 v2, v2, v10, s[10:11]
	v_cndmask_b32_e64 v3, v3, v11, s[10:11]
	v_cndmask_b32_e64 v4, v4, v12, s[10:11]
	v_cmp_gt_f32_e32 vcc, v33, v6
	v_cmp_gt_f32_e64 s[6:7], v49, v7
	v_cmp_gt_f32_e64 s[8:9], v65, v8
	v_cmp_gt_f32_e64 s[10:11], v17, v5
	s_cmp_eq_u32 s15, 3
	v_cndmask_b32_e32 v98, v6, v33, vcc
	v_cndmask_b32_e64 v93, v7, v49, s[6:7]
	v_cndmask_b32_e64 v89, v8, v65, s[8:9]
	v_cndmask_b32_e64 v85, v5, v17, s[10:11]
	v_cndmask_b32_e32 v81, v9, v100, vcc
	v_cndmask_b32_e32 v97, v13, v30, vcc
	v_cndmask_b32_e32 v95, v18, v31, vcc
	v_cndmask_b32_e32 v94, v19, v32, vcc
	v_cndmask_b32_e64 v80, v20, v100, s[6:7]
	v_cndmask_b32_e64 v92, v21, v46, s[6:7]
	v_cndmask_b32_e64 v91, v22, v47, s[6:7]
	v_cndmask_b32_e64 v90, v23, v48, s[6:7]
	v_cndmask_b32_e64 v74, v24, v100, s[8:9]
	v_cndmask_b32_e64 v88, v25, v62, s[8:9]
	v_cndmask_b32_e64 v87, v26, v63, s[8:9]
	v_cndmask_b32_e64 v86, v27, v64, s[8:9]
	v_cndmask_b32_e64 v75, v28, v100, s[10:11]
	v_cndmask_b32_e64 v84, v2, v14, s[10:11]
	v_cndmask_b32_e64 v82, v3, v15, s[10:11]
	v_cndmask_b32_e64 v83, v4, v16, s[10:11]
	s_cbranch_scc0 .LBB5_64
	s_mov_b32 s53, 0
	s_lshl_b32 s52, s5, 7
	s_add_i32 s6, s50, 35
	s_mov_b32 s7, s53
	v_lshl_add_u64 v[10:11], s[52:53], 2, v[78:79]
	s_lshl_b64 s[6:7], s[6:7], 11
	global_load_dwordx4 v[2:5], v[10:11], off offset:448
	global_load_dwordx4 v[6:9], v[10:11], off offset:480
	global_load_dwordx4 v[16:19], v[10:11], off offset:384
	global_load_dwordx4 v[20:23], v[10:11], off offset:416
	v_lshl_add_u64 v[10:11], v[76:77], 0, s[6:7]
	global_load_dwordx4 v[100:103], v[10:11], off
	global_load_dwordx4 v[104:107], v[10:11], off offset:16
	ds_read_b128 v[24:27], v96
	ds_read_b128 v[28:31], v96 offset:16
	ds_read_b128 v[108:111], v96 offset:16896
	ds_read_b128 v[112:115], v96 offset:16912
	ds_read_b128 v[116:119], v96 offset:33792
	ds_read_b128 v[120:123], v96 offset:33808
	ds_read_b128 v[124:127], v96 offset:50688
	ds_read_b128 v[128:131], v96 offset:50704
	ds_read_b128 v[136:139], v96 offset:64
	ds_read_b128 v[140:143], v96 offset:80
	ds_read_b128 v[144:147], v96 offset:16960
	ds_read_b128 v[152:155], v96 offset:16976
	ds_read_b128 v[156:159], v96 offset:33856
	ds_read_b128 v[160:163], v96 offset:33872
	ds_read_b128 v[164:167], v96 offset:50752
	ds_read_b128 v[168:171], v96 offset:50768
	s_brev_b32 s6, 35
	s_waitcnt vmcnt(5)
	v_pk_mul_f32 v[10:11], v[2:3], s[6:7] op_sel_hi:[1,0]
	s_waitcnt vmcnt(4)
	v_pk_mul_f32 v[14:15], v[6:7], s[6:7] op_sel_hi:[1,0]
	s_waitcnt vmcnt(3)
	v_pk_mul_f32 v[2:3], v[16:17], s[6:7] op_sel_hi:[1,0]
	s_waitcnt vmcnt(2)
	v_pk_mul_f32 v[6:7], v[20:21], s[6:7] op_sel_hi:[1,0]
	v_pk_mul_f32 v[16:17], v[8:9], s[6:7] op_sel_hi:[1,0]
	v_pk_mul_f32 v[12:13], v[4:5], s[6:7] op_sel_hi:[1,0]
	v_pk_mul_f32 v[8:9], v[22:23], s[6:7] op_sel_hi:[1,0]
	v_pk_mul_f32 v[4:5], v[18:19], s[6:7] op_sel_hi:[1,0]
	s_waitcnt lgkmcnt(14)
	s_nop 0
	v_mfma_f32_32x32x16_f16 v[50:65], v[70:73], v[24:27], v[2:17]
	v_mfma_f32_32x32x16_f16 v[50:65], v[66:69], v[28:31], v[50:65]
	v_mfma_f32_32x32x16_f16 v[50:65], v[66:69], v[24:27], v[50:65]
	s_waitcnt lgkmcnt(13)
	v_mfma_f32_32x32x16_f16 v[34:49], v[70:73], v[108:111], v[2:17]
	s_waitcnt lgkmcnt(11)
	v_mfma_f32_32x32x16_f16 v[18:33], v[70:73], v[116:119], v[2:17]
	s_waitcnt lgkmcnt(9)
	v_mfma_f32_32x32x16_f16 v[2:17], v[70:73], v[124:127], v[2:17]
	v_mfma_f32_32x32x16_f16 v[34:49], v[66:69], v[112:115], v[34:49]
	v_mfma_f32_32x32x16_f16 v[18:33], v[66:69], v[120:123], v[18:33]
	s_waitcnt lgkmcnt(8)
	v_mfma_f32_32x32x16_f16 v[2:17], v[66:69], v[128:131], v[2:17]
	v_mfma_f32_32x32x16_f16 v[34:49], v[66:69], v[108:111], v[34:49]
	v_mfma_f32_32x32x16_f16 v[18:33], v[66:69], v[116:119], v[18:33]
	v_mfma_f32_32x32x16_f16 v[2:17], v[66:69], v[124:127], v[2:17]
	s_add_i32 s6, s50, 0x43
	s_mov_b32 s7, s53
	s_lshl_b64 s[6:7], s[6:7], 11
	v_lshl_add_u64 v[70:71], v[76:77], 0, s[6:7]
	global_load_dwordx4 v[66:69], v[70:71], off
	s_nop 0
	global_load_dwordx4 v[70:73], v[70:71], off offset:16
	ds_read_b128 v[108:111], v96 offset:128
	ds_read_b128 v[112:115], v96 offset:144
	ds_read_b128 v[116:119], v96 offset:17024
	ds_read_b128 v[120:123], v96 offset:17040
	ds_read_b128 v[124:127], v96 offset:33920
	ds_read_b128 v[128:131], v96 offset:33936
	ds_read_b128 v[172:175], v96 offset:50816
	ds_read_b128 v[176:179], v96 offset:50832
	s_waitcnt vmcnt(2) lgkmcnt(14)
	v_mfma_f32_32x32x16_f16 v[50:65], v[104:107], v[136:139], v[50:65]
	s_waitcnt lgkmcnt(13)
	v_mfma_f32_32x32x16_f16 v[34:49], v[104:107], v[144:147], v[34:49]
	s_waitcnt lgkmcnt(11)
	v_mfma_f32_32x32x16_f16 v[18:33], v[104:107], v[156:159], v[18:33]
	s_waitcnt lgkmcnt(9)
	v_mfma_f32_32x32x16_f16 v[2:17], v[104:107], v[164:167], v[2:17]
	v_mfma_f32_32x32x16_f16 v[50:65], v[100:103], v[140:143], v[50:65]
	v_mfma_f32_32x32x16_f16 v[34:49], v[100:103], v[152:155], v[34:49]
	v_mfma_f32_32x32x16_f16 v[18:33], v[100:103], v[160:163], v[18:33]
	s_waitcnt lgkmcnt(8)
	v_mfma_f32_32x32x16_f16 v[2:17], v[100:103], v[168:171], v[2:17]
	v_mfma_f32_32x32x16_f16 v[50:65], v[100:103], v[136:139], v[50:65]
	v_mfma_f32_32x32x16_f16 v[34:49], v[100:103], v[144:147], v[34:49]
	v_mfma_f32_32x32x16_f16 v[18:33], v[100:103], v[156:159], v[18:33]
	v_mfma_f32_32x32x16_f16 v[2:17], v[100:103], v[164:167], v[2:17]
	s_add_i32 s6, s50, 0x63
	s_mov_b32 s7, s53
	s_lshl_b64 s[6:7], s[6:7], 11
	v_lshl_add_u64 v[78:79], v[76:77], 0, s[6:7]
	global_load_dwordx4 v[100:103], v[78:79], off
	global_load_dwordx4 v[104:107], v[78:79], off offset:16
	ds_read_b128 v[136:139], v96 offset:192
	ds_read_b128 v[140:143], v96 offset:208
	ds_read_b128 v[144:147], v96 offset:17088
	ds_read_b128 v[152:155], v96 offset:17104
	ds_read_b128 v[156:159], v96 offset:33984
	ds_read_b128 v[160:163], v96 offset:34000
	ds_read_b128 v[164:167], v96 offset:50880
	ds_read_b128 v[168:171], v96 offset:50896
	s_waitcnt vmcnt(2) lgkmcnt(14)
	v_mfma_f32_32x32x16_f16 v[50:65], v[70:73], v[108:111], v[50:65]
	s_waitcnt lgkmcnt(13)
	v_mfma_f32_32x32x16_f16 v[34:49], v[70:73], v[116:119], v[34:49]
	s_waitcnt lgkmcnt(11)
	v_mfma_f32_32x32x16_f16 v[18:33], v[70:73], v[124:127], v[18:33]
	s_waitcnt lgkmcnt(9)
	v_mfma_f32_32x32x16_f16 v[2:17], v[70:73], v[172:175], v[2:17]
	v_mfma_f32_32x32x16_f16 v[50:65], v[66:69], v[112:115], v[50:65]
	v_mfma_f32_32x32x16_f16 v[34:49], v[66:69], v[120:123], v[34:49]
	v_mfma_f32_32x32x16_f16 v[18:33], v[66:69], v[128:131], v[18:33]
	s_waitcnt lgkmcnt(8)
	v_mfma_f32_32x32x16_f16 v[2:17], v[66:69], v[176:179], v[2:17]
	v_mfma_f32_32x32x16_f16 v[50:65], v[66:69], v[108:111], v[50:65]
	v_mfma_f32_32x32x16_f16 v[34:49], v[66:69], v[116:119], v[34:49]
	v_mfma_f32_32x32x16_f16 v[18:33], v[66:69], v[124:127], v[18:33]
	v_mfma_f32_32x32x16_f16 v[2:17], v[66:69], v[172:175], v[2:17]
	s_add_i32 s6, s50, 0x83
	s_mov_b32 s7, s53
	s_lshl_b64 s[6:7], s[6:7], 11
	v_lshl_add_u64 v[70:71], v[76:77], 0, s[6:7]
	global_load_dwordx4 v[66:69], v[70:71], off
	s_nop 0
	global_load_dwordx4 v[70:73], v[70:71], off offset:16
	ds_read_b128 v[108:111], v96 offset:256
	ds_read_b128 v[112:115], v96 offset:272
	ds_read_b128 v[116:119], v96 offset:17152
	ds_read_b128 v[120:123], v96 offset:17168
	ds_read_b128 v[124:127], v96 offset:34048
	ds_read_b128 v[128:131], v96 offset:34064
	ds_read_b128 v[172:175], v96 offset:50944
	ds_read_b128 v[176:179], v96 offset:50960
	s_waitcnt vmcnt(2) lgkmcnt(14)
	v_mfma_f32_32x32x16_f16 v[50:65], v[104:107], v[136:139], v[50:65]
	s_waitcnt lgkmcnt(13)
	v_mfma_f32_32x32x16_f16 v[34:49], v[104:107], v[144:147], v[34:49]
	s_waitcnt lgkmcnt(11)
	v_mfma_f32_32x32x16_f16 v[18:33], v[104:107], v[156:159], v[18:33]
	s_waitcnt lgkmcnt(9)
	v_mfma_f32_32x32x16_f16 v[2:17], v[104:107], v[164:167], v[2:17]
	v_mfma_f32_32x32x16_f16 v[50:65], v[100:103], v[140:143], v[50:65]
	v_mfma_f32_32x32x16_f16 v[34:49], v[100:103], v[152:155], v[34:49]
	v_mfma_f32_32x32x16_f16 v[18:33], v[100:103], v[160:163], v[18:33]
	s_waitcnt lgkmcnt(8)
	v_mfma_f32_32x32x16_f16 v[2:17], v[100:103], v[168:171], v[2:17]
	v_mfma_f32_32x32x16_f16 v[50:65], v[100:103], v[136:139], v[50:65]
	v_mfma_f32_32x32x16_f16 v[34:49], v[100:103], v[144:147], v[34:49]
	v_mfma_f32_32x32x16_f16 v[18:33], v[100:103], v[156:159], v[18:33]
	v_mfma_f32_32x32x16_f16 v[2:17], v[100:103], v[164:167], v[2:17]
	s_add_i32 s6, s50, 0xa3
	s_mov_b32 s7, s53
	s_lshl_b64 s[6:7], s[6:7], 11
	v_lshl_add_u64 v[78:79], v[76:77], 0, s[6:7]
	global_load_dwordx4 v[100:103], v[78:79], off
	global_load_dwordx4 v[104:107], v[78:79], off offset:16
	ds_read_b128 v[136:139], v96 offset:320
	ds_read_b128 v[140:143], v96 offset:336
	ds_read_b128 v[144:147], v96 offset:17216
	ds_read_b128 v[152:155], v96 offset:17232
	ds_read_b128 v[156:159], v96 offset:34112
	ds_read_b128 v[160:163], v96 offset:34128
	ds_read_b128 v[164:167], v96 offset:51008
	ds_read_b128 v[168:171], v96 offset:51024
	s_waitcnt vmcnt(2) lgkmcnt(14)
	v_mfma_f32_32x32x16_f16 v[50:65], v[70:73], v[108:111], v[50:65]
	s_waitcnt lgkmcnt(13)
	v_mfma_f32_32x32x16_f16 v[34:49], v[70:73], v[116:119], v[34:49]
	s_waitcnt lgkmcnt(11)
	v_mfma_f32_32x32x16_f16 v[18:33], v[70:73], v[124:127], v[18:33]
	s_waitcnt lgkmcnt(9)
	v_mfma_f32_32x32x16_f16 v[2:17], v[70:73], v[172:175], v[2:17]
	v_mfma_f32_32x32x16_f16 v[50:65], v[66:69], v[112:115], v[50:65]
	v_mfma_f32_32x32x16_f16 v[34:49], v[66:69], v[120:123], v[34:49]
	v_mfma_f32_32x32x16_f16 v[18:33], v[66:69], v[128:131], v[18:33]
	s_waitcnt lgkmcnt(8)
	v_mfma_f32_32x32x16_f16 v[2:17], v[66:69], v[176:179], v[2:17]
	v_mfma_f32_32x32x16_f16 v[50:65], v[66:69], v[108:111], v[50:65]
	v_mfma_f32_32x32x16_f16 v[34:49], v[66:69], v[116:119], v[34:49]
	v_mfma_f32_32x32x16_f16 v[18:33], v[66:69], v[124:127], v[18:33]
	v_mfma_f32_32x32x16_f16 v[2:17], v[66:69], v[172:175], v[2:17]
	s_add_i32 s6, s50, 0xc3
	s_mov_b32 s7, s53
	s_lshl_b64 s[6:7], s[6:7], 11
	v_lshl_add_u64 v[70:71], v[76:77], 0, s[6:7]
	global_load_dwordx4 v[66:69], v[70:71], off
	s_nop 0
	global_load_dwordx4 v[70:73], v[70:71], off offset:16
	ds_read_b128 v[108:111], v96 offset:384
	ds_read_b128 v[112:115], v96 offset:400
	ds_read_b128 v[116:119], v96 offset:17280
	ds_read_b128 v[120:123], v96 offset:17296
	ds_read_b128 v[124:127], v96 offset:34176
	ds_read_b128 v[128:131], v96 offset:34192
	ds_read_b128 v[172:175], v96 offset:51072
	ds_read_b128 v[176:179], v96 offset:51088
	s_waitcnt vmcnt(2) lgkmcnt(14)
	v_mfma_f32_32x32x16_f16 v[50:65], v[104:107], v[136:139], v[50:65]
	s_waitcnt lgkmcnt(13)
	v_mfma_f32_32x32x16_f16 v[34:49], v[104:107], v[144:147], v[34:49]
	s_waitcnt lgkmcnt(11)
	v_mfma_f32_32x32x16_f16 v[18:33], v[104:107], v[156:159], v[18:33]
	s_waitcnt lgkmcnt(9)
	v_mfma_f32_32x32x16_f16 v[2:17], v[104:107], v[164:167], v[2:17]
	v_mfma_f32_32x32x16_f16 v[50:65], v[100:103], v[140:143], v[50:65]
	v_mfma_f32_32x32x16_f16 v[34:49], v[100:103], v[152:155], v[34:49]
	v_mfma_f32_32x32x16_f16 v[18:33], v[100:103], v[160:163], v[18:33]
	s_waitcnt lgkmcnt(8)
	v_mfma_f32_32x32x16_f16 v[2:17], v[100:103], v[168:171], v[2:17]
	v_mfma_f32_32x32x16_f16 v[50:65], v[100:103], v[136:139], v[50:65]
	v_mfma_f32_32x32x16_f16 v[34:49], v[100:103], v[144:147], v[34:49]
	v_mfma_f32_32x32x16_f16 v[18:33], v[100:103], v[156:159], v[18:33]
	v_mfma_f32_32x32x16_f16 v[2:17], v[100:103], v[164:167], v[2:17]
	s_add_i32 s6, s50, 0xe3
	s_mov_b32 s7, s53
	s_lshl_b64 s[6:7], s[6:7], 11
	v_lshl_add_u64 v[100:101], v[76:77], 0, s[6:7]
	global_load_dwordx4 v[76:79], v[100:101], off
	s_nop 0
	global_load_dwordx4 v[100:103], v[100:101], off offset:16
	ds_read_b128 v[104:107], v96 offset:448
	ds_read_b128 v[136:139], v96 offset:464
	ds_read_b128 v[140:143], v96 offset:17344
	ds_read_b128 v[144:147], v96 offset:17360
	ds_read_b128 v[152:155], v96 offset:34240
	ds_read_b128 v[156:159], v96 offset:34256
	ds_read_b128 v[160:163], v96 offset:51136
	ds_read_b128 v[164:167], v96 offset:51152
	s_waitcnt vmcnt(2) lgkmcnt(14)
	v_mfma_f32_32x32x16_f16 v[50:65], v[70:73], v[108:111], v[50:65]
	s_waitcnt lgkmcnt(13)
	v_mfma_f32_32x32x16_f16 v[34:49], v[70:73], v[116:119], v[34:49]
	s_waitcnt lgkmcnt(11)
	v_mfma_f32_32x32x16_f16 v[18:33], v[70:73], v[124:127], v[18:33]
	s_waitcnt lgkmcnt(9)
	v_mfma_f32_32x32x16_f16 v[2:17], v[70:73], v[172:175], v[2:17]
	v_mfma_f32_32x32x16_f16 v[50:65], v[66:69], v[112:115], v[50:65]
	v_mfma_f32_32x32x16_f16 v[34:49], v[66:69], v[120:123], v[34:49]
	v_mfma_f32_32x32x16_f16 v[18:33], v[66:69], v[128:131], v[18:33]
	s_waitcnt lgkmcnt(8)
	v_mfma_f32_32x32x16_f16 v[2:17], v[66:69], v[176:179], v[2:17]
	v_mfma_f32_32x32x16_f16 v[50:65], v[66:69], v[108:111], v[50:65]
	v_mfma_f32_32x32x16_f16 v[34:49], v[66:69], v[116:119], v[34:49]
	v_mfma_f32_32x32x16_f16 v[18:33], v[66:69], v[124:127], v[18:33]
	v_mfma_f32_32x32x16_f16 v[2:17], v[66:69], v[172:175], v[2:17]
	s_waitcnt vmcnt(0) lgkmcnt(7)
	v_mfma_f32_32x32x16_f16 v[50:65], v[100:103], v[104:107], v[50:65]
	s_waitcnt lgkmcnt(5)
	v_mfma_f32_32x32x16_f16 v[34:49], v[100:103], v[140:143], v[34:49]
	s_waitcnt lgkmcnt(3)
	v_mfma_f32_32x32x16_f16 v[18:33], v[100:103], v[152:155], v[18:33]
	s_waitcnt lgkmcnt(1)
	v_mfma_f32_32x32x16_f16 v[2:17], v[100:103], v[160:163], v[2:17]
	v_mfma_f32_32x32x16_f16 v[50:65], v[76:79], v[136:139], v[50:65]
	v_mfma_f32_32x32x16_f16 v[34:49], v[76:79], v[144:147], v[34:49]
	v_mfma_f32_32x32x16_f16 v[18:33], v[76:79], v[156:159], v[18:33]
	s_waitcnt lgkmcnt(0)
	v_mfma_f32_32x32x16_f16 v[2:17], v[76:79], v[164:167], v[2:17]
	v_mfma_f32_32x32x16_f16 v[50:65], v[76:79], v[104:107], v[50:65]
	v_mfma_f32_32x32x16_f16 v[34:49], v[76:79], v[140:143], v[34:49]
	v_mfma_f32_32x32x16_f16 v[18:33], v[76:79], v[152:155], v[18:33]
	v_mfma_f32_32x32x16_f16 v[2:17], v[76:79], v[160:163], v[2:17]
	s_nop 8
	v_max_f32_e32 v53, v53, v53
	v_max_f32_e32 v66, v52, v52
	v_max_f32_e32 v53, v66, v53
	v_max3_f32 v53, v50, v51, v53
	v_max_f32_e32 v57, v57, v57
	v_max_f32_e32 v66, v56, v56
	v_cmp_gt_f32_e64 s[36:37], v53, v98
	v_max_f32_e32 v57, v66, v57
	v_max3_f32 v57, v54, v55, v57
	v_cndmask_b32_e64 v53, v98, v53, s[36:37]
	v_cndmask_b32_e64 v50, v97, v50, s[36:37]
	v_cmp_gt_f32_e64 s[8:9], v57, v53
	s_nop 1
	v_cndmask_b32_e64 v53, v53, v57, s[8:9]
	v_cndmask_b32_e64 v50, v50, v54, s[8:9]
	v_max_f32_e32 v54, v61, v61
	v_max_f32_e32 v57, v60, v60
	v_max_f32_e32 v54, v57, v54
	v_max3_f32 v54, v58, v59, v54
	v_cmp_gt_f32_e64 s[14:15], v54, v53
	v_max_f32_e32 v57, v64, v64
	s_nop 0
	v_cndmask_b32_e64 v53, v53, v54, s[14:15]
	v_max_f32_e32 v54, v65, v65
	v_max_f32_e32 v54, v57, v54
	v_max3_f32 v54, v62, v63, v54
	v_cndmask_b32_e64 v50, v50, v58, s[14:15]
	v_cmp_gt_f32_e64 s[20:21], v54, v53
	s_nop 1
	v_cndmask_b32_e64 v53, v53, v54, s[20:21]
	v_cndmask_b32_e64 v50, v50, v62, s[20:21]
	v_cmp_neq_f32_e32 vcc, v50, v53
	v_mov_b32_e32 v50, 0
	v_mov_b32_e32 v54, 0
	s_and_saveexec_b64 s[6:7], vcc
	s_cbranch_execz .LBB5_69
	v_cndmask_b32_e64 v51, v95, v51, s[36:37]
	v_cndmask_b32_e64 v51, v51, v55, s[8:9]
	v_cndmask_b32_e64 v51, v51, v59, s[14:15]
	v_cndmask_b32_e64 v51, v51, v63, s[20:21]
	v_cmp_neq_f32_e32 vcc, v51, v53
	v_mov_b32_e32 v54, 1
	s_and_saveexec_b64 s[10:11], vcc
	v_cndmask_b32_e64 v51, v94, v52, s[36:37]
	v_cndmask_b32_e64 v51, v51, v56, s[8:9]
	v_cndmask_b32_e64 v51, v51, v60, s[14:15]
	v_cndmask_b32_e64 v51, v51, v64, s[20:21]
	v_cmp_eq_f32_e32 vcc, v51, v53
	s_nop 1
	v_cndmask_b32_e64 v54, 3, 2, vcc
	s_or_b64 exec, exec, s[10:11]
